# grid-barrier poll rewrite (1 round trip/poll), L1 ds_read hoist into fresh VGPRs, slim LSTM software barrier; k_gcn moved to .text
# speedup vs baseline: 1.0124x; 1.0124x over previous
.LBB1_15:
	ds_read_b32 v3, v1
	s_mov_b64 s[4:5], -1
	s_waitcnt lgkmcnt(0)
	v_readfirstlane_b32 s3, v3
	s_cmp_gt_i32 s3, 3
	s_cbranch_scc1 .LBB1_14
	s_mov_b64 s[4:5], 0
	s_sleep 1
	s_branch .LBB1_14

.LBB1_22:
	ds_read_b32 v4, v3
	s_mov_b64 s[4:5], -1
	s_waitcnt lgkmcnt(0)
	v_readfirstlane_b32 s3, v4
	s_cmp_gt_i32 s3, 7
	s_cbranch_scc1 .LBB1_21
	s_mov_b64 s[4:5], 0
	s_sleep 1
	s_branch .LBB1_21

.LBB1_78:
	ds_read_b32 v3, v2
	s_mov_b64 s[4:5], -1
	s_waitcnt lgkmcnt(0)
	v_readfirstlane_b32 s3, v3
	s_cmp_gt_i32 s3, 11
	s_cbranch_scc1 .LBB1_77
	s_mov_b64 s[4:5], 0
	s_sleep 1
	s_branch .LBB1_77

.Lgb1_poll:
	global_load_dword v114, v2, s[42:43] offset:3072 sc1
	global_load_dword v3, v2, s[42:43] offset:2048 sc1
	s_waitcnt vmcnt(0)
	v_cmp_le_i32_e32 vcc, s69, v3
	s_cbranch_vccnz .LBB1_98
	v_cmp_ne_u32_e32 vcc, 0, v114
	s_cbranch_vccnz .Lgb1_fail
	s_add_i32 s3, s3, -1
	s_cmp_lg_u32 s3, 0
	s_cbranch_scc0 .Lgb1_fail
	s_sleep 2
	s_branch .Lgb1_poll
.Lgb1_fail:
	s_mov_b64 s[8:9], -1
	s_branch .LBB1_101

.LBB1_109:
	ds_read_b32 v3, v2
	s_mov_b64 s[6:7], -1
	s_waitcnt lgkmcnt(0)
	v_readfirstlane_b32 s3, v3
	s_cmp_gt_i32 s3, 15
	s_cbranch_scc1 .LBB1_108
	s_mov_b64 s[6:7], 0
	s_sleep 1
	s_branch .LBB1_108

.LBB1_125:
	ds_read_b32 v65, v5
	s_mov_b64 s[16:17], -1
	s_waitcnt lgkmcnt(0)
	v_readfirstlane_b32 s3, v65
	s_cmp_gt_i32 s3, 19
	s_cbranch_scc1 .LBB1_124
	s_mov_b64 s[16:17], 0
	s_sleep 1
	s_branch .LBB1_124

.LBB1_142:
	ds_read_b32 v3, v2
	s_mov_b64 s[16:17], -1
	s_waitcnt lgkmcnt(0)
	v_readfirstlane_b32 s3, v3
	s_cmp_gt_i32 s3, 23
	s_cbranch_scc1 .LBB1_141
	s_mov_b64 s[16:17], 0
	s_sleep 1
	s_branch .LBB1_141

.LBB1_149:
	ds_read_b32 v3, v2
	s_mov_b64 s[16:17], -1
	s_waitcnt lgkmcnt(0)
	v_readfirstlane_b32 s3, v3
	s_cmp_gt_i32 s3, 27
	s_cbranch_scc1 .LBB1_148
	s_mov_b64 s[16:17], 0
	s_sleep 1
	s_branch .LBB1_148

.Lgb2_poll:
	global_load_dword v114, v2, s[42:43] offset:3072 sc1
	global_load_dword v3, v2, s[42:43] offset:2304 sc1
	s_waitcnt vmcnt(0)
	v_cmp_le_i32_e32 vcc, s69, v3
	s_cbranch_vccnz .LBB1_169
	v_cmp_ne_u32_e32 vcc, 0, v114
	s_cbranch_vccnz .Lgb2_fail
	s_add_i32 s3, s3, -1
	s_cmp_lg_u32 s3, 0
	s_cbranch_scc0 .Lgb2_fail
	s_sleep 2
	s_branch .Lgb2_poll
.Lgb2_fail:
	s_mov_b64 s[18:19], -1
	s_branch .LBB1_173

.LBB1_181:
	ds_read_b32 v3, v2
	s_mov_b64 s[16:17], -1
	s_waitcnt lgkmcnt(0)
	v_readfirstlane_b32 s3, v3
	s_cmp_gt_i32 s3, 31
	s_cbranch_scc1 .LBB1_180
	s_mov_b64 s[16:17], 0
	s_sleep 1
	s_branch .LBB1_180

.LBB1_191:
	ds_read_b32 v4, v3
	s_waitcnt lgkmcnt(0)
	v_readfirstlane_b32 s18, v4
	s_cmp_gt_i32 s18, 35
	s_mov_b64 s[18:19], -1
	s_cbranch_scc1 .LBB1_190
	s_mov_b64 s[18:19], 0
	s_sleep 1
	s_branch .LBB1_190

.LBB1_217:
	ds_read_b32 v5, v4
	s_waitcnt lgkmcnt(0)
	v_readfirstlane_b32 s34, v5
	s_cmp_gt_i32 s34, 39
	s_mov_b64 s[34:35], -1
	s_cbranch_scc1 .LBB1_216
	s_mov_b64 s[34:35], 0
	s_sleep 1
	s_branch .LBB1_216

.LBB1_229:
	ds_read_b32 v5, v4
	s_waitcnt lgkmcnt(0)
	v_readfirstlane_b32 s6, v5
	s_cmp_gt_i32 s6, 43
	s_mov_b64 s[6:7], -1
	s_cbranch_scc1 .LBB1_228
	s_mov_b64 s[6:7], 0
	s_sleep 1
	s_branch .LBB1_228

.LBB1_259:
	ds_read_b32 v2, v1
	s_mov_b64 s[6:7], -1
	s_waitcnt lgkmcnt(0)
	v_readfirstlane_b32 s3, v2
	s_cmp_gt_i32 s3, 47
	s_cbranch_scc1 .LBB1_258
	s_mov_b64 s[6:7], 0
	s_sleep 1
	s_branch .LBB1_258

.LBB1_272:
	ds_read_b32 v3, v2
	s_waitcnt lgkmcnt(0)
	v_readfirstlane_b32 s2, v3
	s_cmp_gt_i32 s2, 51
	s_mov_b64 s[2:3], -1
	s_cbranch_scc1 .LBB1_271
	s_mov_b64 s[2:3], 0
	s_sleep 1
	s_branch .LBB1_271

.Lgb3_poll:
	global_load_dword v114, v2, s[42:43] offset:3072 sc1
	global_load_dword v3, v2, s[42:43] offset:2560 sc1
	s_waitcnt vmcnt(0)
	v_cmp_le_i32_e32 vcc, s69, v3
	s_cbranch_vccnz .LBB1_292
	v_cmp_ne_u32_e32 vcc, 0, v114
	s_cbranch_vccnz .Lgb3_fail
	s_add_i32 s8, s8, -1
	s_cmp_lg_u32 s8, 0
	s_cbranch_scc0 .Lgb3_fail
	s_sleep 2
	s_branch .Lgb3_poll
.Lgb3_fail:
	s_mov_b64 s[4:5], -1
	s_branch .LBB1_296

.LBB1_304:
	ds_read_b32 v3, v2
	s_waitcnt lgkmcnt(0)
	v_readfirstlane_b32 s2, v3
	s_cmp_gt_i32 s2, 55
	s_mov_b64 s[2:3], -1
	s_cbranch_scc1 .LBB1_303
	s_mov_b64 s[2:3], 0
	s_sleep 1
	s_branch .LBB1_303

.LBB1_358:
	ds_read_b32 v27, v26
	s_waitcnt lgkmcnt(0)
	v_readfirstlane_b32 s4, v27
	s_cmp_gt_i32 s4, 59
	s_mov_b64 s[4:5], -1
	s_cbranch_scc1 .LBB1_357
	s_mov_b64 s[4:5], 0
	s_sleep 1
	s_branch .LBB1_357

.LBB1_371:
	s_cmp_eq_u32 s9, 0
	s_cbranch_scc1 .LBB1_392
	s_add_i32 s6, s9, -1
	s_bitcmp1_b32 s6, 0
	s_cselect_b32 s7, 0x2800, 0
	v_add_u32_e32 v59, s7, v1
	ds_read_b128 v[60:63], v59
	ds_read_b128 v[64:67], v59 offset:5120
	s_bitcmp1_b32 s9, 0
	s_cselect_b32 s10, 0x2800, 0
	s_cmp_eq_u32 s6, 23
	s_waitcnt lgkmcnt(1)
	v_mfma_f32_16x16x32_f16 v[70:73], v[2:5], v[60:63], v[18:21]
	v_mfma_f32_16x16x32_f16 v[74:77], v[22:25], v[60:63], v[38:41]
	v_add_u32_e32 v60, s10, v1
	ds_read_b128 v[78:81], v60 offset:20480
	ds_read_b128 v[82:85], v60 offset:25600
	s_cselect_b64 s[10:11], -1, 0
	s_waitcnt lgkmcnt(2)
	v_mfma_f32_16x16x32_f16 v[70:73], v[6:9], v[64:67], v[70:73]
	s_cmp_lg_u32 s6, 23
	v_mfma_f32_16x16x32_f16 v[62:65], v[26:29], v[64:67], v[74:77]
	s_waitcnt lgkmcnt(1)
	v_mfma_f32_16x16x32_f16 v[70:73], v[10:13], v[78:81], v[70:73]
	v_mfma_f32_16x16x32_f16 v[62:65], v[30:33], v[78:81], v[62:65]
	s_waitcnt lgkmcnt(0)
	v_mfma_f32_16x16x32_f16 v[70:73], v[14:17], v[82:85], v[70:73]
	v_mfma_f32_16x16x32_f16 v[62:65], v[34:37], v[82:85], v[62:65]
	ds_read_b128 v[86:89], v59 offset:256
	ds_read_b128 v[90:93], v59 offset:5376
	ds_read_b128 v[94:97], v60 offset:20736
	ds_read_b128 v[98:101], v60 offset:25856
	s_nop 2
	v_exp_f32_e32 v67, v72
	v_exp_f32_e32 v66, v64
	v_exp_f32_e32 v53, v70
	v_exp_f32_e32 v52, v62
	v_exp_f32_e32 v71, v71
	v_exp_f32_e32 v70, v63
	v_pk_add_f32 v[62:63], v[66:67], 1.0 op_sel_hi:[1,0]
	v_pk_fma_f32 v[66:67], v[66:67], s[8:9], v[68:69] op_sel_hi:[1,0,0]
	v_pk_fma_f32 v[52:53], v[52:53], v[62:63], v[62:63]
	v_pk_fma_f32 v[66:67], v[66:67], v[70:71], v[66:67]
	v_fma_f32 v58, v71, v53, v53
	v_fma_f32 v61, v70, v52, v52
	v_rcp_f32_e32 v63, v58
	v_rcp_f32_e32 v62, v61
	v_pk_fma_f32 v[42:43], v[42:43], v[52:53], v[66:67]
	v_exp_f32_e32 v61, v73
	v_exp_f32_e32 v64, v65
	v_pk_mul_f32 v[42:43], v[42:43], v[62:63]
	v_add_u32_e32 v58, s7, v54
	v_exp_f32_e32 v52, v43
	v_exp_f32_e32 v53, v42
	s_nop 0
	v_pk_add_f32 v[52:53], v[52:53], 1.0 op_sel_hi:[1,0]
	s_nop 0
	v_fma_f32 v61, v61, v52, v52
	v_pk_add_f32 v[62:63], v[52:53], 2.0 op_sel_hi:[1,0] neg_lo:[1,0] neg_hi:[1,0]
	v_fmac_f32_e32 v53, v64, v53
	v_rcp_f32_e32 v52, v61
	v_rcp_f32_e32 v53, v53
	s_nop 0
	v_pk_mul_f32 v[52:53], v[62:63], v[52:53]
	s_nop 0
	v_cvt_pk_f16_f32 v61, v52, v53
	ds_write_b32 v58, v61 offset:20480
	s_cbranch_scc1 .LBB1_376
	v_and_b32_e32 v61, 64, v57
	v_add_f32_e32 v52, v52, v53
	v_xor_b32_e32 v53, 16, v57
	v_add_u32_e32 v61, 64, v61
	v_cmp_lt_i32_e32 vcc, v53, v61
	v_add_f32_e32 v52, 0, v52
	s_nop 0
	v_cndmask_b32_e32 v53, v57, v53, vcc
	v_lshlrev_b32_e32 v53, 2, v53
	ds_bpermute_b32 v53, v53, v52
	s_waitcnt lgkmcnt(0)
	v_add_f32_e32 v52, v52, v53
	v_xor_b32_e32 v53, 32, v57
	v_cmp_lt_i32_e32 vcc, v53, v61
	s_nop 1
	v_cndmask_b32_e32 v53, v57, v53, vcc
	v_lshlrev_b32_e32 v53, 2, v53
	ds_bpermute_b32 v53, v53, v52
	s_and_saveexec_b64 s[6:7], s[4:5]
	s_cbranch_execz .LBB1_375
	s_waitcnt lgkmcnt(0)
	v_add_f32_e32 v52, v52, v53
	v_add_u32_e32 v53, s12, v55
	ds_write_b32 v53, v52

.LBB1_376:
	s_andn2_b64 vcc, exec, s[10:11]
	s_waitcnt lgkmcnt(1)
	v_mfma_f32_16x16x32_f16 v[74:77], v[2:5], v[86:89], v[18:21]
	v_mfma_f32_16x16x32_f16 v[62:65], v[22:25], v[86:89], v[38:41]
	v_mfma_f32_16x16x32_f16 v[74:77], v[6:9], v[90:93], v[74:77]
	v_mfma_f32_16x16x32_f16 v[62:65], v[26:29], v[90:93], v[62:65]
	v_mfma_f32_16x16x32_f16 v[74:77], v[10:13], v[94:97], v[74:77]
	v_mfma_f32_16x16x32_f16 v[62:65], v[30:33], v[94:97], v[62:65]
	v_mfma_f32_16x16x32_f16 v[74:77], v[14:17], v[98:101], v[74:77]
	v_mfma_f32_16x16x32_f16 v[62:65], v[34:37], v[98:101], v[62:65]
	ds_read_b128 v[102:105], v59 offset:512
	ds_read_b128 v[106:109], v59 offset:5632
	ds_read_b128 v[110:113], v60 offset:20992
	ds_read_b128 v[114:117], v60 offset:26112
	s_nop 2
	v_exp_f32_e32 v67, v76
	v_exp_f32_e32 v66, v64
	v_exp_f32_e32 v53, v74
	v_exp_f32_e32 v52, v62
	v_exp_f32_e32 v71, v75
	v_exp_f32_e32 v70, v63
	v_pk_add_f32 v[62:63], v[66:67], 1.0 op_sel_hi:[1,0]
	v_pk_fma_f32 v[66:67], v[66:67], s[8:9], v[68:69] op_sel_hi:[1,0,0]
	v_pk_fma_f32 v[52:53], v[52:53], v[62:63], v[62:63]
	v_pk_fma_f32 v[66:67], v[66:67], v[70:71], v[66:67]
	v_fma_f32 v61, v71, v53, v53
	v_rcp_f32_e32 v63, v61
	v_fma_f32 v61, v70, v52, v52
	v_rcp_f32_e32 v62, v61
	v_pk_fma_f32 v[44:45], v[44:45], v[52:53], v[66:67]
	v_exp_f32_e32 v61, v77
	v_exp_f32_e32 v64, v65
	v_pk_mul_f32 v[44:45], v[44:45], v[62:63]
	s_nop 0
	v_exp_f32_e32 v52, v45
	v_exp_f32_e32 v53, v44
	s_nop 0
	v_pk_add_f32 v[52:53], v[52:53], 1.0 op_sel_hi:[1,0]
	s_nop 0
	v_fma_f32 v61, v61, v52, v52
	v_pk_add_f32 v[62:63], v[52:53], 2.0 op_sel_hi:[1,0] neg_lo:[1,0] neg_hi:[1,0]
	v_fmac_f32_e32 v53, v64, v53
	v_rcp_f32_e32 v52, v61
	v_rcp_f32_e32 v53, v53
	v_cndmask_b32_e64 v61, 0, 1, s[10:11]
	v_cmp_ne_u32_e64 s[6:7], 1, v61
	v_pk_mul_f32 v[52:53], v[62:63], v[52:53]
	s_nop 0
	v_cvt_pk_f16_f32 v61, v52, v53
	ds_write_b32 v58, v61 offset:20736
	s_cbranch_vccnz .LBB1_380
	v_and_b32_e32 v61, 64, v57
	v_add_f32_e32 v52, v52, v53
	v_xor_b32_e32 v53, 16, v57
	v_add_u32_e32 v61, 64, v61
	v_cmp_lt_i32_e32 vcc, v53, v61
	v_add_f32_e32 v52, 0, v52
	s_nop 0
	v_cndmask_b32_e32 v53, v57, v53, vcc
	v_lshlrev_b32_e32 v53, 2, v53
	ds_bpermute_b32 v53, v53, v52
	s_waitcnt lgkmcnt(0)
	v_add_f32_e32 v52, v52, v53
	v_xor_b32_e32 v53, 32, v57
	v_cmp_lt_i32_e32 vcc, v53, v61
	s_nop 1
	v_cndmask_b32_e32 v53, v57, v53, vcc
	v_lshlrev_b32_e32 v53, 2, v53
	ds_bpermute_b32 v53, v53, v52
	s_and_saveexec_b64 s[10:11], s[4:5]
	s_cbranch_execz .LBB1_379
	s_waitcnt lgkmcnt(0)
	v_add_f32_e32 v52, v52, v53
	v_add_u32_e32 v53, s12, v55
	ds_write_b32 v53, v52 offset:64

.LBB1_380:
	s_and_b64 vcc, exec, s[6:7]
	s_waitcnt lgkmcnt(1)
	v_mfma_f32_16x16x32_f16 v[74:77], v[2:5], v[102:105], v[18:21]
	v_mfma_f32_16x16x32_f16 v[62:65], v[22:25], v[102:105], v[38:41]
	v_mfma_f32_16x16x32_f16 v[74:77], v[6:9], v[106:109], v[74:77]
	v_mfma_f32_16x16x32_f16 v[62:65], v[26:29], v[106:109], v[62:65]
	v_mfma_f32_16x16x32_f16 v[74:77], v[10:13], v[110:113], v[74:77]
	v_mfma_f32_16x16x32_f16 v[62:65], v[30:33], v[110:113], v[62:65]
	v_mfma_f32_16x16x32_f16 v[74:77], v[14:17], v[114:117], v[74:77]
	v_mfma_f32_16x16x32_f16 v[62:65], v[34:37], v[114:117], v[62:65]
	ds_read_b128 v[86:89], v59 offset:768
	ds_read_b128 v[90:93], v59 offset:5888
	ds_read_b128 v[94:97], v60 offset:21248
	ds_read_b128 v[98:101], v60 offset:26368
	s_nop 2
	v_exp_f32_e32 v67, v76
	v_exp_f32_e32 v66, v64
	v_exp_f32_e32 v53, v74
	v_exp_f32_e32 v52, v62
	v_exp_f32_e32 v71, v75
	v_exp_f32_e32 v70, v63
	v_pk_add_f32 v[62:63], v[66:67], 1.0 op_sel_hi:[1,0]
	v_pk_fma_f32 v[66:67], v[66:67], s[8:9], v[68:69] op_sel_hi:[1,0,0]
	v_pk_fma_f32 v[52:53], v[52:53], v[62:63], v[62:63]
	v_pk_fma_f32 v[66:67], v[66:67], v[70:71], v[66:67]
	v_fma_f32 v61, v71, v53, v53
	v_rcp_f32_e32 v63, v61
	v_fma_f32 v61, v70, v52, v52
	v_rcp_f32_e32 v62, v61
	v_pk_fma_f32 v[46:47], v[46:47], v[52:53], v[66:67]
	v_exp_f32_e32 v61, v77
	v_exp_f32_e32 v64, v65
	v_pk_mul_f32 v[46:47], v[46:47], v[62:63]
	s_nop 0
	v_exp_f32_e32 v52, v47
	v_exp_f32_e32 v53, v46
	s_nop 0
	v_pk_add_f32 v[52:53], v[52:53], 1.0 op_sel_hi:[1,0]
	s_nop 0
	v_fma_f32 v61, v61, v52, v52
	v_pk_add_f32 v[62:63], v[52:53], 2.0 op_sel_hi:[1,0] neg_lo:[1,0] neg_hi:[1,0]
	v_fmac_f32_e32 v53, v64, v53
	v_rcp_f32_e32 v52, v61
	v_rcp_f32_e32 v53, v53
	s_nop 0
	v_pk_mul_f32 v[52:53], v[62:63], v[52:53]
	s_nop 0
	v_cvt_pk_f16_f32 v61, v52, v53
	ds_write_b32 v58, v61 offset:20992
	s_cbranch_vccnz .LBB1_384
	v_and_b32_e32 v61, 64, v57
	v_add_f32_e32 v52, v52, v53
	v_xor_b32_e32 v53, 16, v57
	v_add_u32_e32 v61, 64, v61
	v_cmp_lt_i32_e32 vcc, v53, v61
	v_add_f32_e32 v52, 0, v52
	s_nop 0
	v_cndmask_b32_e32 v53, v57, v53, vcc
	v_lshlrev_b32_e32 v53, 2, v53
	ds_bpermute_b32 v53, v53, v52
	s_waitcnt lgkmcnt(0)
	v_add_f32_e32 v52, v52, v53
	v_xor_b32_e32 v53, 32, v57
	v_cmp_lt_i32_e32 vcc, v53, v61
	s_nop 1
	v_cndmask_b32_e32 v53, v57, v53, vcc
	v_lshlrev_b32_e32 v53, 2, v53
	ds_bpermute_b32 v53, v53, v52
	s_and_saveexec_b64 s[10:11], s[4:5]
	s_cbranch_execz .LBB1_383
	s_waitcnt lgkmcnt(0)
	v_add_f32_e32 v52, v52, v53
	v_add_u32_e32 v53, s12, v55
	ds_write_b32 v53, v52 offset:128

.LBB1_384:
	s_and_b64 vcc, exec, s[6:7]
	s_waitcnt lgkmcnt(1)
	v_mfma_f32_16x16x32_f16 v[74:77], v[2:5], v[86:89], v[18:21]
	v_mfma_f32_16x16x32_f16 v[62:65], v[22:25], v[86:89], v[38:41]
	v_mfma_f32_16x16x32_f16 v[74:77], v[6:9], v[90:93], v[74:77]
	v_mfma_f32_16x16x32_f16 v[62:65], v[26:29], v[90:93], v[62:65]
	v_mfma_f32_16x16x32_f16 v[74:77], v[10:13], v[94:97], v[74:77]
	v_mfma_f32_16x16x32_f16 v[62:65], v[30:33], v[94:97], v[62:65]
	v_mfma_f32_16x16x32_f16 v[74:77], v[14:17], v[98:101], v[74:77]
	v_mfma_f32_16x16x32_f16 v[62:65], v[34:37], v[98:101], v[62:65]
	ds_read_b128 v[102:105], v59 offset:1024
	ds_read_b128 v[106:109], v59 offset:6144
	ds_read_b128 v[110:113], v60 offset:21504
	ds_read_b128 v[114:117], v60 offset:26624
	s_nop 2
	v_exp_f32_e32 v67, v76
	v_exp_f32_e32 v66, v64
	v_exp_f32_e32 v53, v74
	v_exp_f32_e32 v52, v62
	v_exp_f32_e32 v71, v75
	v_exp_f32_e32 v70, v63
	v_pk_add_f32 v[62:63], v[66:67], 1.0 op_sel_hi:[1,0]
	v_pk_fma_f32 v[66:67], v[66:67], s[8:9], v[68:69] op_sel_hi:[1,0,0]
	v_pk_fma_f32 v[52:53], v[52:53], v[62:63], v[62:63]
	v_pk_fma_f32 v[66:67], v[66:67], v[70:71], v[66:67]
	v_fma_f32 v61, v71, v53, v53
	v_rcp_f32_e32 v63, v61
	v_fma_f32 v61, v70, v52, v52
	v_rcp_f32_e32 v62, v61
	v_pk_fma_f32 v[48:49], v[48:49], v[52:53], v[66:67]
	v_exp_f32_e32 v61, v77
	v_exp_f32_e32 v64, v65
	v_pk_mul_f32 v[48:49], v[48:49], v[62:63]
	s_nop 0
	v_exp_f32_e32 v52, v49
	v_exp_f32_e32 v53, v48
	s_nop 0
	v_pk_add_f32 v[52:53], v[52:53], 1.0 op_sel_hi:[1,0]
	s_nop 0
	v_fma_f32 v61, v61, v52, v52
	v_pk_add_f32 v[62:63], v[52:53], 2.0 op_sel_hi:[1,0] neg_lo:[1,0] neg_hi:[1,0]
	v_fmac_f32_e32 v53, v64, v53
	v_rcp_f32_e32 v52, v61
	v_rcp_f32_e32 v53, v53
	s_nop 0
	v_pk_mul_f32 v[52:53], v[62:63], v[52:53]
	s_nop 0
	v_cvt_pk_f16_f32 v61, v52, v53
	ds_write_b32 v58, v61 offset:21248
	s_cbranch_vccnz .LBB1_388
	v_and_b32_e32 v61, 64, v57
	v_add_f32_e32 v52, v52, v53
	v_xor_b32_e32 v53, 16, v57
	v_add_u32_e32 v61, 64, v61
	v_cmp_lt_i32_e32 vcc, v53, v61
	v_add_f32_e32 v52, 0, v52
	s_nop 0
	v_cndmask_b32_e32 v53, v57, v53, vcc
	v_lshlrev_b32_e32 v53, 2, v53
	ds_bpermute_b32 v53, v53, v52
	s_waitcnt lgkmcnt(0)
	v_add_f32_e32 v52, v52, v53
	v_xor_b32_e32 v53, 32, v57
	v_cmp_lt_i32_e32 vcc, v53, v61
	s_nop 1
	v_cndmask_b32_e32 v53, v57, v53, vcc
	v_lshlrev_b32_e32 v53, 2, v53
	ds_bpermute_b32 v53, v53, v52
	s_and_saveexec_b64 s[10:11], s[4:5]
	s_cbranch_execz .LBB1_387
	s_waitcnt lgkmcnt(0)
	v_add_f32_e32 v52, v52, v53
	v_add_u32_e32 v53, s12, v55
	ds_write_b32 v53, v52 offset:192

.LBB1_388:
	s_and_b64 vcc, exec, s[6:7]
	s_waitcnt lgkmcnt(1)
	v_mfma_f32_16x16x32_f16 v[74:77], v[2:5], v[102:105], v[18:21]
	v_mfma_f32_16x16x32_f16 v[60:63], v[22:25], v[102:105], v[38:41]
	v_mfma_f32_16x16x32_f16 v[74:77], v[6:9], v[106:109], v[74:77]
	v_mfma_f32_16x16x32_f16 v[60:63], v[26:29], v[106:109], v[60:63]
	v_mfma_f32_16x16x32_f16 v[74:77], v[10:13], v[110:113], v[74:77]
	v_mfma_f32_16x16x32_f16 v[60:63], v[30:33], v[110:113], v[60:63]
	v_mfma_f32_16x16x32_f16 v[74:77], v[14:17], v[114:117], v[74:77]
	v_mfma_f32_16x16x32_f16 v[60:63], v[34:37], v[114:117], v[60:63]
	s_nop 6
	v_exp_f32_e32 v65, v76
	v_exp_f32_e32 v64, v62
	v_exp_f32_e32 v53, v74
	v_exp_f32_e32 v52, v60
	v_exp_f32_e32 v67, v75
	v_exp_f32_e32 v66, v61
	v_pk_add_f32 v[60:61], v[64:65], 1.0 op_sel_hi:[1,0]
	v_pk_fma_f32 v[64:65], v[64:65], s[8:9], v[68:69] op_sel_hi:[1,0,0]
	v_pk_fma_f32 v[52:53], v[52:53], v[60:61], v[60:61]
	v_pk_fma_f32 v[64:65], v[64:65], v[66:67], v[64:65]
	v_fma_f32 v59, v67, v53, v53
	v_rcp_f32_e32 v61, v59
	v_fma_f32 v59, v66, v52, v52
	v_rcp_f32_e32 v60, v59
	v_pk_fma_f32 v[50:51], v[50:51], v[52:53], v[64:65]
	v_exp_f32_e32 v59, v77
	v_exp_f32_e32 v62, v63
	v_pk_mul_f32 v[50:51], v[50:51], v[60:61]
	s_nop 0
	v_exp_f32_e32 v52, v51
	v_exp_f32_e32 v53, v50
	s_nop 0
	v_pk_add_f32 v[52:53], v[52:53], 1.0 op_sel_hi:[1,0]
	s_nop 0
	v_fma_f32 v59, v59, v52, v52
	v_pk_add_f32 v[60:61], v[52:53], 2.0 op_sel_hi:[1,0] neg_lo:[1,0] neg_hi:[1,0]
	v_fmac_f32_e32 v53, v62, v53
	v_rcp_f32_e32 v52, v59
	v_rcp_f32_e32 v53, v53
	s_nop 0
	v_pk_mul_f32 v[52:53], v[60:61], v[52:53]
	s_nop 0
	v_cvt_pk_f16_f32 v59, v52, v53
	ds_write_b32 v58, v59 offset:21504
	s_cbranch_vccnz .LBB1_392
	v_and_b32_e32 v58, 64, v57
	v_add_f32_e32 v52, v52, v53
	v_xor_b32_e32 v53, 16, v57
	v_add_u32_e32 v58, 64, v58
	v_cmp_lt_i32_e32 vcc, v53, v58
	v_add_f32_e32 v52, 0, v52
	s_nop 0
	v_cndmask_b32_e32 v53, v57, v53, vcc
	v_lshlrev_b32_e32 v53, 2, v53
	ds_bpermute_b32 v53, v53, v52
	s_waitcnt lgkmcnt(0)
	v_add_f32_e32 v52, v52, v53
	v_xor_b32_e32 v53, 32, v57
	v_cmp_lt_i32_e32 vcc, v53, v58
	s_nop 1
	v_cndmask_b32_e32 v53, v57, v53, vcc
	v_lshlrev_b32_e32 v53, 2, v53
	ds_bpermute_b32 v53, v53, v52
	s_and_saveexec_b64 s[6:7], s[4:5]
	s_cbranch_execz .LBB1_391
	s_waitcnt lgkmcnt(0)
	v_add_f32_e32 v52, v52, v53
	v_add_u32_e32 v53, s12, v55
	ds_write_b32 v53, v52 offset:256

.LBB1_392:
	s_waitcnt lgkmcnt(0)
	s_mov_b64 exec, 1
	v_mov_b32_e32 v52, 1
	ds_add_u32 v56, v52
	s_mov_b64 exec, -1
	s_add_i32 s9, s9, 1
	s_mul_i32 s10, s9, 12
	s_setprio 0
.Lb1_poll:
	ds_read_b32 v52, v56
	s_waitcnt lgkmcnt(0)
	v_readfirstlane_b32 s6, v52
	s_cmp_ge_i32 s6, s10
	s_cbranch_scc1 .LBB1_370
	s_sleep 1
	s_branch .Lb1_poll

.LBB1_427:
	s_waitcnt lgkmcnt(0)
	s_mov_b64 exec, 1
	v_mov_b32_e32 v70, 1
	ds_add_u32 v75, v70
	s_mov_b64 exec, -1
	s_add_i32 s7, s7, 1
	s_mul_i32 s9, s7, 12
	s_setprio 0
.Lb0_poll:
	ds_read_b32 v70, v75
	s_waitcnt lgkmcnt(0)
	v_readfirstlane_b32 s10, v70
	s_cmp_ge_i32 s10, s9
	s_cbranch_scc1 .LBB1_424
	s_sleep 1
	s_branch .Lb0_poll

	.amdhsa_kernel _Z11k_lstm_mfmaPKfS0_S0_S0_S0_S0_S0_S0_S0_Pf6WkArgs
		.amdhsa_group_segment_fixed_size 134696
		.amdhsa_private_segment_fixed_size 0
		.amdhsa_kernarg_size 488
		.amdhsa_user_sgpr_count 2
		.amdhsa_user_sgpr_dispatch_ptr 0
		.amdhsa_user_sgpr_queue_ptr 0
		.amdhsa_user_sgpr_kernarg_segment_ptr 1
		.amdhsa_user_sgpr_dispatch_id 0
		.amdhsa_user_sgpr_kernarg_preload_length 0
		.amdhsa_user_sgpr_kernarg_preload_offset 0
		.amdhsa_user_sgpr_private_segment_size 0
		.amdhsa_uses_dynamic_stack 0
		.amdhsa_enable_private_segment 0
		.amdhsa_system_sgpr_workgroup_id_x 1
		.amdhsa_system_sgpr_workgroup_id_y 0
		.amdhsa_system_sgpr_workgroup_id_z 0
		.amdhsa_system_sgpr_workgroup_info 0
		.amdhsa_system_vgpr_workitem_id 0
		.amdhsa_next_free_vgpr 118
		.amdhsa_next_free_sgpr 96
		.amdhsa_accum_offset 120
		.amdhsa_reserve_vcc 1
		.amdhsa_float_round_mode_32 0
		.amdhsa_float_round_mode_16_64 0
		.amdhsa_float_denorm_mode_32 3
		.amdhsa_float_denorm_mode_16_64 3
		.amdhsa_dx10_clamp 1
		.amdhsa_ieee_mode 1
		.amdhsa_fp16_overflow 0
		.amdhsa_tg_split 0
		.amdhsa_exception_fp_ieee_invalid_op 0
		.amdhsa_exception_fp_denorm_src 0
		.amdhsa_exception_fp_ieee_div_zero 0
		.amdhsa_exception_fp_ieee_overflow 0
		.amdhsa_exception_fp_ieee_underflow 0
		.amdhsa_exception_fp_ieee_inexact 0
		.amdhsa_exception_int_div_zero 0
	.end_amdhsa_kernel

	.text
	.protected	_Z5k_gcnILi128ELb1ELi16EEvPKDv8_DF16_PKiS4_PKfS2_S6_PDF16_S6_S6_S2_S6_S2_S6_S6_S6_PfS4_
	.globl	_Z5k_gcnILi128ELb1ELi16EEvPKDv8_DF16_PKiS4_PKfS2_S6_PDF16_S6_S6_S2_S6_S2_S6_S6_S6_PfS4_
	.p2align	8
	.type	_Z5k_gcnILi128ELb1ELi16EEvPKDv8_DF16_PKiS4_PKfS2_S6_PDF16_S6_S6_S2_S6_S2_S6_S6_S6_PfS4_,@function

	.amdhsa_kernel _Z5k_gcnILi128ELb1ELi16EEvPKDv8_DF16_PKiS4_PKfS2_S6_PDF16_S6_S6_S2_S6_S2_S6_S6_S6_PfS4_
		.amdhsa_group_segment_fixed_size 12288
		.amdhsa_private_segment_fixed_size 0
		.amdhsa_kernarg_size 136
		.amdhsa_user_sgpr_count 2
		.amdhsa_user_sgpr_dispatch_ptr 0
		.amdhsa_user_sgpr_queue_ptr 0
		.amdhsa_user_sgpr_kernarg_segment_ptr 1
		.amdhsa_user_sgpr_dispatch_id 0
		.amdhsa_user_sgpr_kernarg_preload_length 0
		.amdhsa_user_sgpr_kernarg_preload_offset 0
		.amdhsa_user_sgpr_private_segment_size 0
		.amdhsa_uses_dynamic_stack 0
		.amdhsa_enable_private_segment 0
		.amdhsa_system_sgpr_workgroup_id_x 1
		.amdhsa_system_sgpr_workgroup_id_y 0
		.amdhsa_system_sgpr_workgroup_id_z 0
		.amdhsa_system_sgpr_workgroup_info 0
		.amdhsa_system_vgpr_workitem_id 0
		.amdhsa_next_free_vgpr 96
		.amdhsa_next_free_sgpr 34
		.amdhsa_accum_offset 96
		.amdhsa_reserve_vcc 1
		.amdhsa_float_round_mode_32 0
		.amdhsa_float_round_mode_16_64 0
		.amdhsa_float_denorm_mode_32 3
		.amdhsa_float_denorm_mode_16_64 3
		.amdhsa_dx10_clamp 1
		.amdhsa_ieee_mode 1
		.amdhsa_fp16_overflow 0
		.amdhsa_tg_split 0
		.amdhsa_exception_fp_ieee_invalid_op 0
		.amdhsa_exception_fp_denorm_src 0
		.amdhsa_exception_fp_ieee_div_zero 0
		.amdhsa_exception_fp_ieee_overflow 0
		.amdhsa_exception_fp_ieee_underflow 0
		.amdhsa_exception_fp_ieee_inexact 0
		.amdhsa_exception_int_div_zero 0
	.end_amdhsa_kernel
	.text
.Lfunc_end2:
	.size	_Z5k_gcnILi128ELb1ELi16EEvPKDv8_DF16_PKiS4_PKfS2_S6_PDF16_S6_S6_S2_S6_S2_S6_S6_S6_PfS4_, .Lfunc_end2-_Z5k_gcnILi128ELb1ELi16EEvPKDv8_DF16_PKiS4_PKfS2_S6_PDF16_S6_S6_S2_S6_S2_S6_S6_S6_PfS4_
	.set _Z5k_gcnILi128ELb1ELi16EEvPKDv8_DF16_PKiS4_PKfS2_S6_PDF16_S6_S6_S2_S6_S2_S6_S6_S6_PfS4_.num_vgpr, 96
	.set _Z5k_gcnILi128ELb1ELi16EEvPKDv8_DF16_PKiS4_PKfS2_S6_PDF16_S6_S6_S2_S6_S2_S6_S6_S6_PfS4_.num_agpr, 0
	.set _Z5k_gcnILi128ELb1ELi16EEvPKDv8_DF16_PKiS4_PKfS2_S6_PDF16_S6_S6_S2_S6_S2_S6_S6_S6_PfS4_.numbered_sgpr, 34
	.set _Z5k_gcnILi128ELb1ELi16EEvPKDv8_DF16_PKiS4_PKfS2_S6_PDF16_S6_S6_S2_S6_S2_S6_S6_S6_PfS4_.num_named_barrier, 0
	.set _Z5k_gcnILi128ELb1ELi16EEvPKDv8_DF16_PKiS4_PKfS2_S6_PDF16_S6_S6_S2_S6_S2_S6_S6_S6_PfS4_.private_seg_size, 0
	.set _Z5k_gcnILi128ELb1ELi16EEvPKDv8_DF16_PKiS4_PKfS2_S6_PDF16_S6_S6_S2_S6_S2_S6_S6_S6_PfS4_.uses_vcc, 1
	.set _Z5k_gcnILi128ELb1ELi16EEvPKDv8_DF16_PKiS4_PKfS2_S6_PDF16_S6_S6_S2_S6_S2_S6_S6_S6_PfS4_.uses_flat_scratch, 0
	.set _Z5k_gcnILi128ELb1ELi16EEvPKDv8_DF16_PKiS4_PKfS2_S6_PDF16_S6_S6_S2_S6_S2_S6_S6_S6_PfS4_.has_dyn_sized_stack, 0
	.set _Z5k_gcnILi128ELb1ELi16EEvPKDv8_DF16_PKiS4_PKfS2_S6_PDF16_S6_S6_S2_S6_S2_S6_S6_S6_PfS4_.has_recursion, 0
	.set _Z5k_gcnILi128ELb1ELi16EEvPKDv8_DF16_PKiS4_PKfS2_S6_PDF16_S6_S6_S2_S6_S2_S6_S6_S6_PfS4_.has_indirect_call, 0

amdhsa.kernels:
  - .agpr_count:     0
    .args:
      - .actual_access:  read_only
        .address_space:  global
        .offset:         0
        .size:           8
        .value_kind:     global_buffer
      - .actual_access:  read_only
        .address_space:  global
        .offset:         8
        .size:           8
        .value_kind:     global_buffer
      - .actual_access:  read_only
        .address_space:  global
        .offset:         16
        .size:           8
        .value_kind:     global_buffer
      - .actual_access:  read_only
        .address_space:  global
        .offset:         24
        .size:           8
        .value_kind:     global_buffer
      - .actual_access:  read_only
        .address_space:  global
        .offset:         32
        .size:           8
        .value_kind:     global_buffer
      - .actual_access:  read_only
        .address_space:  global
        .offset:         40
        .size:           8
        .value_kind:     global_buffer
      - .actual_access:  read_only
        .address_space:  global
        .offset:         48
        .size:           8
        .value_kind:     global_buffer
      - .actual_access:  read_only
        .address_space:  global
        .offset:         56
        .size:           8
        .value_kind:     global_buffer
      - .actual_access:  write_only
        .address_space:  global
        .offset:         64
        .size:           8
        .value_kind:     global_buffer
      - .actual_access:  write_only
        .address_space:  global
        .offset:         72
        .size:           8
        .value_kind:     global_buffer
      - .actual_access:  write_only
        .address_space:  global
        .offset:         80
        .size:           8
        .value_kind:     global_buffer
      - .actual_access:  write_only
        .address_space:  global
        .offset:         88
        .size:           8
        .value_kind:     global_buffer
      - .address_space:  global
        .offset:         96
        .size:           8
        .value_kind:     global_buffer
      - .address_space:  global
        .offset:         104
        .size:           8
        .value_kind:     global_buffer
      - .address_space:  global
        .offset:         112
        .size:           8
        .value_kind:     global_buffer
      - .address_space:  global
        .offset:         120
        .size:           8
        .value_kind:     global_buffer
      - .actual_access:  read_only
        .address_space:  global
        .offset:         128
        .size:           8
        .value_kind:     global_buffer
      - .actual_access:  write_only
        .address_space:  global
        .offset:         136
        .size:           8
        .value_kind:     global_buffer
    .group_segment_fixed_size: 84096
    .kernarg_segment_align: 8
    .kernarg_segment_size: 144
    .language:       OpenCL C
    .language_version:
      - 2
      - 0
    .max_flat_workgroup_size: 1024
    .name:           _Z14k_csr_fallbackPKiS0_S0_PKfS2_S2_S2_S2_PDv8_DF16_S4_S4_S4_PiS5_PfS4_S2_PDF16_
    .private_segment_fixed_size: 0
    .sgpr_count:     50
    .sgpr_spill_count: 0
    .symbol:         _Z14k_csr_fallbackPKiS0_S0_PKfS2_S2_S2_S2_PDv8_DF16_S4_S4_S4_PiS5_PfS4_S2_PDF16_.kd
    .uniform_work_group_size: 1
    .uses_dynamic_stack: false
    .vgpr_count:     93
    .vgpr_spill_count: 0
    .wavefront_size: 64
  - .agpr_count:     0
    .args:
      - .actual_access:  read_only
        .address_space:  global
        .offset:         0
        .size:           8
        .value_kind:     global_buffer
      - .actual_access:  read_only
        .address_space:  global
        .offset:         8
        .size:           8
        .value_kind:     global_buffer
      - .actual_access:  read_only
        .address_space:  global
        .offset:         16
        .size:           8
        .value_kind:     global_buffer
      - .actual_access:  read_only
        .address_space:  global
        .offset:         24
        .size:           8
        .value_kind:     global_buffer
      - .actual_access:  read_only
        .address_space:  global
        .offset:         32
        .size:           8
        .value_kind:     global_buffer
      - .actual_access:  read_only
        .address_space:  global
        .offset:         40
        .size:           8
        .value_kind:     global_buffer
      - .actual_access:  read_only
        .address_space:  global
        .offset:         48
        .size:           8
        .value_kind:     global_buffer
      - .actual_access:  read_only
        .address_space:  global
        .offset:         56
        .size:           8
        .value_kind:     global_buffer
      - .actual_access:  read_only
        .address_space:  global
        .offset:         64
        .size:           8
        .value_kind:     global_buffer
      - .actual_access:  write_only
        .address_space:  global
        .offset:         72
        .size:           8
        .value_kind:     global_buffer
      - .offset:         80
        .size:           152
        .value_kind:     by_value
      - .offset:         232
        .size:           4
        .value_kind:     hidden_block_count_x
      - .offset:         236
        .size:           4
        .value_kind:     hidden_block_count_y
      - .offset:         240
        .size:           4
        .value_kind:     hidden_block_count_z
      - .offset:         244
        .size:           2
        .value_kind:     hidden_group_size_x
      - .offset:         246
        .size:           2
        .value_kind:     hidden_group_size_y
      - .offset:         248
        .size:           2
        .value_kind:     hidden_group_size_z
      - .offset:         250
        .size:           2
        .value_kind:     hidden_remainder_x
      - .offset:         252
        .size:           2
        .value_kind:     hidden_remainder_y
      - .offset:         254
        .size:           2
        .value_kind:     hidden_remainder_z
      - .offset:         272
        .size:           8
        .value_kind:     hidden_global_offset_x
      - .offset:         280
        .size:           8
        .value_kind:     hidden_global_offset_y
      - .offset:         288
        .size:           8
        .value_kind:     hidden_global_offset_z
      - .offset:         296
        .size:           2
        .value_kind:     hidden_grid_dims
    .group_segment_fixed_size: 134696
    .kernarg_segment_align: 8
    .kernarg_segment_size: 488
    .language:       OpenCL C
    .language_version:
      - 2
      - 0
    .max_flat_workgroup_size: 1024
    .name:           _Z11k_lstm_mfmaPKfS0_S0_S0_S0_S0_S0_S0_S0_Pf6WkArgs
    .private_segment_fixed_size: 0
    .sgpr_count:     76
    .sgpr_spill_count: 0
    .symbol:         _Z11k_lstm_mfmaPKfS0_S0_S0_S0_S0_S0_S0_S0_Pf6WkArgs.kd
    .uniform_work_group_size: 1
    .uses_dynamic_stack: false
    .vgpr_count:     118
    .vgpr_spill_count: 0
    .wavefront_size: 64
  - .agpr_count:     0
    .args:
      - .actual_access:  read_only
        .address_space:  global
        .offset:         0
        .size:           8
        .value_kind:     global_buffer
      - .actual_access:  read_only
        .address_space:  global
        .offset:         8
        .size:           8
        .value_kind:     global_buffer
      - .actual_access:  read_only
        .address_space:  global
        .offset:         16
        .size:           8
        .value_kind:     global_buffer
      - .actual_access:  read_only
        .address_space:  global
        .offset:         24
        .size:           8
        .value_kind:     global_buffer
      - .actual_access:  read_only
        .address_space:  global
        .offset:         32
        .size:           8
        .value_kind:     global_buffer
      - .actual_access:  read_only
        .address_space:  global
        .offset:         40
        .size:           8
        .value_kind:     global_buffer
      - .actual_access:  read_only
        .address_space:  global
        .offset:         48
        .size:           8
        .value_kind:     global_buffer
      - .actual_access:  read_only
        .address_space:  global
        .offset:         56
        .size:           8
        .value_kind:     global_buffer
      - .actual_access:  read_only
        .address_space:  global
        .offset:         64
        .size:           8
        .value_kind:     global_buffer
      - .actual_access:  read_only
        .address_space:  global
        .offset:         72
        .size:           8
        .value_kind:     global_buffer
      - .actual_access:  read_only
        .address_space:  global
        .offset:         80
        .size:           8
        .value_kind:     global_buffer
      - .actual_access:  read_only
        .address_space:  global
        .offset:         88
        .size:           8
        .value_kind:     global_buffer
      - .actual_access:  read_only
        .address_space:  global
        .offset:         96
        .size:           8
        .value_kind:     global_buffer
      - .actual_access:  read_only
        .address_space:  global
        .offset:         104
        .size:           8
        .value_kind:     global_buffer
      - .actual_access:  read_only
        .address_space:  global
        .offset:         112
        .size:           8
        .value_kind:     global_buffer
      - .actual_access:  write_only
        .address_space:  global
        .offset:         120
        .size:           8
        .value_kind:     global_buffer
      - .actual_access:  read_only
        .address_space:  global
        .offset:         128
        .size:           8
        .value_kind:     global_buffer
    .group_segment_fixed_size: 12288
    .kernarg_segment_align: 8
    .kernarg_segment_size: 136
    .language:       OpenCL C
    .language_version:
      - 2
      - 0
    .max_flat_workgroup_size: 256
    .name:           _Z5k_gcnILi128ELb1ELi16EEvPKDv8_DF16_PKiS4_PKfS2_S6_PDF16_S6_S6_S2_S6_S2_S6_S6_S6_PfS4_
    .private_segment_fixed_size: 0
    .sgpr_count:     40
    .sgpr_spill_count: 0
    .symbol:         _Z5k_gcnILi128ELb1ELi16EEvPKDv8_DF16_PKiS4_PKfS2_S6_PDF16_S6_S6_S2_S6_S2_S6_S6_S6_PfS4_.kd
    .uniform_work_group_size: 1
    .uses_dynamic_stack: false
    .vgpr_count:     96
    .vgpr_spill_count: 0
    .wavefront_size: 64
